# speedup vs baseline: 1.0154x; 1.0154x over previous
.LBB3_36:
	s_andn2_b64 vcc, exec, s[6:7]
	s_cbranch_vccnz .LBB3_86
	s_cmpk_gt_u32 s2, 0xff
	s_cbranch_scc1 .LBB3_86
	s_mov_b64 s[40:41], s[0:1]
	s_mov_b32 s44, s18
	s_mov_b32 s45, s19
	s_mov_b32 s46, 0
	v_mov_b32_e32 v248, v0
.Lgru_tile:
	s_cmp_lg_u32 s46, 0
	s_cbranch_scc1 .Lgru_tile_alt
	s_load_dwordx8 s[8:15], s[0:1], 0x0
	s_load_dwordx2 s[2:3], s[0:1], 0x20
	v_lshlrev_b32_e32 v52, 4, v0
	v_mov_b32_e32 v53, 0
	s_movk_i32 s6, 0x100
	s_waitcnt lgkmcnt(0)
	v_lshl_add_u64 v[30:31], s[14:15], 0, v[52:53]
	v_add_co_u32_e32 v14, vcc, 0x2000, v30
	v_bfe_u32 v55, v0, 6, 2
	s_nop 0
	v_addc_co_u32_e32 v15, vcc, 0, v31, vcc
	v_add_co_u32_e32 v22, vcc, 0x6000, v30
	v_mov_b32_e32 v46, s3
	s_nop 0
	v_addc_co_u32_e32 v23, vcc, 0, v31, vcc
	v_add_co_u32_e32 v32, vcc, 0xa000, v30
	v_mov_b32_e32 v47, s13
	s_nop 0
	v_addc_co_u32_e32 v33, vcc, 0, v31, vcc
	v_add_co_u32_e32 v38, vcc, 0xe000, v30
	v_mov_b32_e32 v48, s12
	s_nop 0
	v_addc_co_u32_e32 v39, vcc, 0, v31, vcc
	v_cmp_gt_u32_e32 vcc, s6, v0
	v_mul_u32_u24_e32 v54, 0x540, v55
	v_mov_b32_e32 v49, v53
	v_cndmask_b32_e32 v47, v46, v47, vcc
	v_mov_b32_e32 v46, s2
	v_cndmask_b32_e32 v46, v46, v48, vcc
	v_lshlrev_b32_e32 v48, 4, v54
	v_lshl_add_u64 v[46:47], v[46:47], 0, v[48:49]
	v_lshlrev_b32_e32 v50, 4, v1
	v_mov_b32_e32 v51, v53
	s_movk_i32 s5, 0x1000
	v_lshl_add_u64 v[46:47], v[46:47], 0, v[50:51]
	v_add_co_u32_e32 v48, vcc, s5, v46
	s_movk_i32 s4, 0x2000
	s_nop 0
	v_addc_co_u32_e32 v49, vcc, 0, v47, vcc
	v_or_b32_e32 v56, 0x400, v0
	v_add_co_u32_e32 v60, vcc, s4, v46
	v_lshlrev_b32_e32 v16, 4, v56
	v_or_b32_e32 v24, 0x8000, v52
	v_or_b32_e32 v34, 0xc000, v52
	v_or_b32_e32 v30, 0x1000, v0
	v_addc_co_u32_e32 v61, vcc, 0, v47, vcc
	s_movk_i32 s2, 0x3000
	global_load_dwordx4 v[2:5], v52, s[14:15]
	global_load_dwordx4 v[6:9], v[14:15], off
	global_load_dwordx4 v[10:13], v16, s[14:15]
	s_nop 0
	global_load_dwordx4 v[14:17], v[22:23], off
	global_load_dwordx4 v[18:21], v24, s[14:15]
	s_nop 0
	global_load_dwordx4 v[22:25], v[32:33], off
	global_load_dwordx4 v[26:29], v34, s[14:15]
	v_lshlrev_b32_e32 v57, 4, v30
	global_load_dwordx4 v[30:33], v[38:39], off
	global_load_dwordx4 v[34:37], v57, s[14:15]
	v_or_b32_e32 v38, 0x1200, v0
	v_add_co_u32_e32 v62, vcc, s2, v46
	v_lshlrev_b32_e32 v58, 4, v38
	v_or_b32_e32 v38, 0x1400, v0
	v_addc_co_u32_e32 v63, vcc, 0, v47, vcc
	s_movk_i32 s2, 0x4000
	v_min_u32_e32 v38, 0x14ff, v38
	v_add_co_u32_e32 v64, vcc, s2, v46
	v_lshlrev_b32_e32 v59, 4, v38
	global_load_dwordx4 v[38:41], v58, s[14:15]
	global_load_dwordx4 v[42:45], v59, s[14:15]
	global_load_dwordx4 v[82:85], v[46:47], off
	global_load_dwordx4 v[86:89], v[46:47], off offset:1024
	global_load_dwordx4 v[90:93], v[46:47], off offset:2048
	global_load_dwordx4 v[94:97], v[46:47], off offset:3072
	global_load_dwordx4 v[98:101], v[48:49], off offset:1024
	global_load_dwordx4 v[102:105], v[48:49], off offset:2048
	global_load_dwordx4 v[106:109], v[60:61], off offset:-4096
	global_load_dwordx4 v[110:113], v[60:61], off
	global_load_dwordx4 v[114:117], v[60:61], off offset:1024
	global_load_dwordx4 v[118:121], v[60:61], off offset:2048
	v_addc_co_u32_e32 v65, vcc, 0, v47, vcc
	global_load_dwordx4 v[122:125], v[60:61], off offset:3072
	global_load_dwordx4 v[126:129], v[64:65], off offset:-4096
	global_load_dwordx4 v[130:133], v[48:49], off offset:3072
	global_load_dwordx4 v[134:137], v[62:63], off offset:1024
	global_load_dwordx4 v[138:141], v[62:63], off offset:2048
	global_load_dwordx4 v[142:145], v[62:63], off offset:3072
	global_load_dwordx4 v[146:149], v[64:65], off
	global_load_dwordx4 v[150:153], v[64:65], off offset:1024
	global_load_dwordx4 v[154:157], v[64:65], off offset:2048
	global_load_dwordx4 v[158:161], v[64:65], off offset:3072
	v_add_co_u32_e32 v46, vcc, 0x5000, v46
	s_movk_i32 s2, 0xff
	s_nop 0
	v_addc_co_u32_e32 v47, vcc, 0, v47, vcc
	global_load_dwordx4 v[162:165], v[46:47], off
.Lgru_after_wloads:
	v_cmp_lt_u32_e64 s[6:7], s2, v0
	v_cmp_gt_u32_e32 vcc, 32, v0
	s_and_saveexec_b64 s[2:3], vcc
	s_cbranch_execz .LBB3_43
	v_or_b32_e32 v46, s18, v0
	v_cmp_gt_i32_e32 vcc, s19, v46
	v_mov_b32_e32 v47, -1
	s_and_saveexec_b64 s[4:5], vcc
	s_cbranch_execz .LBB3_42
	s_movk_i32 s12, 0xf9f
	v_cmp_lt_i32_e32 vcc, s12, v46
	s_and_saveexec_b64 s[12:13], vcc
	s_cbranch_execz .LBB3_41
	s_load_dwordx2 s[14:15], s[0:1], 0x38
	v_mov_b32_e32 v47, 0
	s_waitcnt lgkmcnt(0)
	v_lshl_add_u64 v[46:47], v[46:47], 2, s[14:15]
	v_add_co_u32_e32 v46, vcc, 0xffffd000, v46
	s_nop 1
	v_addc_co_u32_e32 v47, vcc, -1, v47, vcc
	global_load_dword v46, v[46:47], off offset:-3712

.LBB3_53:
	s_or_b64 exec, exec, s[2:3]
	s_movk_i32 s2, 0x80
	v_and_b32_e32 v204, 31, v0
	v_lshrrev_b32_e32 v205, 5, v1
	v_cmp_gt_u32_e64 s[2:3], s2, v0
	s_cmp_lg_u32 s46, 0
	s_cbranch_scc1 .Lgru_skip_sw
	ds_write_b128 v52, v[2:5]
	ds_write_b128 v52, v[6:9] offset:8192
	ds_write_b128 v52, v[10:13] offset:16384
	ds_write_b128 v52, v[14:17] offset:24576
	ds_write_b128 v52, v[18:21] offset:32768
	ds_write_b128 v52, v[22:25] offset:40960
	ds_write_b128 v52, v[26:29] offset:49152
	ds_write_b128 v52, v[30:33] offset:57344
	ds_write_b128 v57, v[34:37]
	ds_write_b128 v58, v[38:41]
	ds_write_b128 v59, v[42:45]
.Lgru_skip_sw:
	s_and_saveexec_b64 s[4:5], s[2:3]
	s_cbranch_execz .LBB3_55
	v_lshlrev_b32_e32 v2, 4, v195
	v_lshl_or_b32 v2, v205, 3, v2
	v_mov_b32_e32 v3, 0x3c00
	v_cmp_eq_u32_e32 vcc, v2, v204
	v_or_b32_e32 v5, 1, v2
	v_or_b32_e32 v4, 2, v2
	v_cndmask_b32_e32 v6, 0, v3, vcc
	v_cmp_eq_u32_e32 vcc, v5, v204
	v_or_b32_e32 v8, 3, v2
	v_or_b32_e32 v9, 6, v2
	v_cndmask_b32_e32 v7, 0, v3, vcc
	v_cmp_eq_u32_e32 vcc, v4, v204
	v_or_b32_e32 v4, 4, v2
	v_or_b32_e32 v10, 5, v2
	v_cndmask_b32_e32 v5, 0, v3, vcc
	v_cmp_eq_u32_e32 vcc, v8, v204
	v_or_b32_e32 v2, 7, v2
	s_nop 0
	v_cndmask_b32_e32 v8, 0, v3, vcc
	v_cmp_eq_u32_e32 vcc, v4, v204
	s_nop 1
	v_cndmask_b32_e32 v4, 0, v3, vcc
	v_cmp_eq_u32_e32 vcc, v9, v204
	s_nop 1
	v_cndmask_b32_e32 v9, 0, v3, vcc
	v_cmp_eq_u32_e32 vcc, v10, v204
	s_nop 1
	v_cndmask_b32_e32 v10, 0, v3, vcc
	v_cmp_eq_u32_e32 vcc, v2, v204
	v_pack_b32_f16 v4, v4, v10
	s_nop 0
	v_cndmask_b32_e32 v2, 0, v3, vcc
	v_pack_b32_f16 v3, v5, v8
	v_pack_b32_f16 v5, v9, v2
	v_pack_b32_f16 v2, v6, v7
	v_lshlrev_b32_e32 v6, 10, v195
	v_lshl_or_b32 v6, v1, 4, v6
	v_add_u32_e32 v6, 0x26280, v6
	ds_write_b128 v6, v[2:5]

.Lgru_tile_end:
	s_mov_b64 exec, -1
	s_addk_i32 s44, 0x2000
	s_cmp_lt_i32 s44, s45
	s_cbranch_scc0 .LBB3_86
	s_mov_b32 s46, 1
	s_mov_b64 s[0:1], s[40:41]
	s_mov_b32 s18, s44
	s_mov_b32 s19, s45
	v_mov_b32_e32 v0, v248
	v_and_b32_e32 v1, 63, v0
	v_lshrrev_b32_e32 v195, 6, v0
	s_waitcnt lgkmcnt(0)
	s_barrier
	s_branch .Lgru_tile

.Lgru_tile_alt:
	s_load_dwordx8 s[8:15], s[0:1], 0x0
	v_lshlrev_b32_e32 v52, 4, v0
	v_mov_b32_e32 v53, 0
	v_bfe_u32 v55, v0, 6, 2
	v_mul_u32_u24_e32 v54, 0x540, v55
	v_lshlrev_b32_e32 v50, 4, v1
	v_or_b32_e32 v56, 0x400, v0
	s_movk_i32 s2, 0xff
	s_waitcnt lgkmcnt(0)
	s_branch .Lgru_after_wloads

	.amdhsa_kernel _Z8gru_mfmaPKiPKDF16_PKDv8_DF16_S5_S5_S5_S0_S0_PfPKfS8_S8_S8_S0_
		.amdhsa_group_segment_fixed_size 160512
		.amdhsa_private_segment_fixed_size 0
		.amdhsa_kernarg_size 112
		.amdhsa_user_sgpr_count 2
		.amdhsa_user_sgpr_dispatch_ptr 0
		.amdhsa_user_sgpr_queue_ptr 0
		.amdhsa_user_sgpr_kernarg_segment_ptr 1
		.amdhsa_user_sgpr_dispatch_id 0
		.amdhsa_user_sgpr_kernarg_preload_length 0
		.amdhsa_user_sgpr_kernarg_preload_offset 0
		.amdhsa_user_sgpr_private_segment_size 0
		.amdhsa_uses_dynamic_stack 0
		.amdhsa_enable_private_segment 0
		.amdhsa_system_sgpr_workgroup_id_x 1
		.amdhsa_system_sgpr_workgroup_id_y 0
		.amdhsa_system_sgpr_workgroup_id_z 0
		.amdhsa_system_sgpr_workgroup_info 0
		.amdhsa_system_vgpr_workitem_id 0
		.amdhsa_next_free_vgpr 256
		.amdhsa_next_free_sgpr 96
		.amdhsa_accum_offset 256
		.amdhsa_reserve_vcc 1
		.amdhsa_float_round_mode_32 0
		.amdhsa_float_round_mode_16_64 0
		.amdhsa_float_denorm_mode_32 3
		.amdhsa_float_denorm_mode_16_64 3
		.amdhsa_dx10_clamp 1
		.amdhsa_ieee_mode 1
		.amdhsa_fp16_overflow 0
		.amdhsa_tg_split 0
		.amdhsa_exception_fp_ieee_invalid_op 0
		.amdhsa_exception_fp_denorm_src 0
		.amdhsa_exception_fp_ieee_div_zero 0
		.amdhsa_exception_fp_ieee_overflow 0
		.amdhsa_exception_fp_ieee_underflow 0
		.amdhsa_exception_fp_ieee_inexact 0
		.amdhsa_exception_int_div_zero 0
	.end_amdhsa_kernel

amdhsa.kernels:
  - .agpr_count:     0
    .args:
      - .actual_access:  write_only
        .address_space:  global
        .offset:         0
        .size:           8
        .value_kind:     global_buffer
      - .offset:         8
        .size:           4
        .value_kind:     by_value
      - .offset:         16
        .size:           4
        .value_kind:     hidden_block_count_x
      - .offset:         20
        .size:           4
        .value_kind:     hidden_block_count_y
      - .offset:         24
        .size:           4
        .value_kind:     hidden_block_count_z
      - .offset:         28
        .size:           2
        .value_kind:     hidden_group_size_x
      - .offset:         30
        .size:           2
        .value_kind:     hidden_group_size_y
      - .offset:         32
        .size:           2
        .value_kind:     hidden_group_size_z
      - .offset:         34
        .size:           2
        .value_kind:     hidden_remainder_x
      - .offset:         36
        .size:           2
        .value_kind:     hidden_remainder_y
      - .offset:         38
        .size:           2
        .value_kind:     hidden_remainder_z
      - .offset:         56
        .size:           8
        .value_kind:     hidden_global_offset_x
      - .offset:         64
        .size:           8
        .value_kind:     hidden_global_offset_y
      - .offset:         72
        .size:           8
        .value_kind:     hidden_global_offset_z
      - .offset:         80
        .size:           2
        .value_kind:     hidden_grid_dims
    .group_segment_fixed_size: 0
    .kernarg_segment_align: 8
    .kernarg_segment_size: 272
    .language:       OpenCL C
    .language_version:
      - 2
      - 0
    .max_flat_workgroup_size: 1024
    .name:           _Z11zero_kernelPDv4_fi
    .private_segment_fixed_size: 0
    .sgpr_count:     11
    .sgpr_spill_count: 0
    .symbol:         _Z11zero_kernelPDv4_fi.kd
    .uniform_work_group_size: 1
    .uses_dynamic_stack: false
    .vgpr_count:     6
    .vgpr_spill_count: 0
    .wavefront_size: 64
  - .agpr_count:     0
    .args:
      - .actual_access:  read_only
        .address_space:  global
        .offset:         0
        .size:           8
        .value_kind:     global_buffer
      - .actual_access:  read_only
        .address_space:  global
        .offset:         8
        .size:           8
        .value_kind:     global_buffer
      - .actual_access:  read_only
        .address_space:  global
        .offset:         16
        .size:           8
        .value_kind:     global_buffer
      - .actual_access:  read_only
        .address_space:  global
        .offset:         24
        .size:           8
        .value_kind:     global_buffer
      - .actual_access:  write_only
        .address_space:  global
        .offset:         32
        .size:           8
        .value_kind:     global_buffer
      - .actual_access:  read_only
        .address_space:  global
        .offset:         40
        .size:           8
        .value_kind:     global_buffer
      - .actual_access:  read_only
        .address_space:  global
        .offset:         48
        .size:           8
        .value_kind:     global_buffer
      - .address_space:  global
        .offset:         56
        .size:           8
        .value_kind:     global_buffer
      - .address_space:  global
        .offset:         64
        .size:           8
        .value_kind:     global_buffer
      - .address_space:  global
        .offset:         72
        .size:           8
        .value_kind:     global_buffer
      - .address_space:  global
        .offset:         80
        .size:           8
        .value_kind:     global_buffer
      - .offset:         88
        .size:           4
        .value_kind:     hidden_block_count_x
      - .offset:         92
        .size:           4
        .value_kind:     hidden_block_count_y
      - .offset:         96
        .size:           4
        .value_kind:     hidden_block_count_z
      - .offset:         100
        .size:           2
        .value_kind:     hidden_group_size_x
      - .offset:         102
        .size:           2
        .value_kind:     hidden_group_size_y
      - .offset:         104
        .size:           2
        .value_kind:     hidden_group_size_z
      - .offset:         106
        .size:           2
        .value_kind:     hidden_remainder_x
      - .offset:         108
        .size:           2
        .value_kind:     hidden_remainder_y
      - .offset:         110
        .size:           2
        .value_kind:     hidden_remainder_z
      - .offset:         128
        .size:           8
        .value_kind:     hidden_global_offset_x
      - .offset:         136
        .size:           8
        .value_kind:     hidden_global_offset_y
      - .offset:         144
        .size:           8
        .value_kind:     hidden_global_offset_z
      - .offset:         152
        .size:           2
        .value_kind:     hidden_grid_dims
    .group_segment_fixed_size: 61528
    .kernarg_segment_align: 8
    .kernarg_segment_size: 344
    .language:       OpenCL C
    .language_version:
      - 2
      - 0
    .max_flat_workgroup_size: 640
    .name:           _Z11p_gemm_mfmaPKfPKDv8_DF16_S0_S0_PDF16_PKiS6_PiS7_S7_S7_
    .private_segment_fixed_size: 0
    .sgpr_count:     36
    .sgpr_spill_count: 0
    .symbol:         _Z11p_gemm_mfmaPKfPKDv8_DF16_S0_S0_PDF16_PKiS6_PiS7_S7_S7_.kd
    .uniform_work_group_size: 1
    .uses_dynamic_stack: false
    .vgpr_count:     156
    .vgpr_spill_count: 0
    .wavefront_size: 64
  - .agpr_count:     0
    .args:
      - .actual_access:  read_only
        .address_space:  global
        .offset:         0
        .size:           8
        .value_kind:     global_buffer
      - .actual_access:  read_only
        .address_space:  global
        .offset:         8
        .size:           8
        .value_kind:     global_buffer
      - .actual_access:  read_only
        .address_space:  global
        .offset:         16
        .size:           8
        .value_kind:     global_buffer
      - .actual_access:  read_only
        .address_space:  global
        .offset:         24
        .size:           8
        .value_kind:     global_buffer
      - .actual_access:  read_only
        .address_space:  global
        .offset:         32
        .size:           8
        .value_kind:     global_buffer
      - .actual_access:  read_only
        .address_space:  global
        .offset:         40
        .size:           8
        .value_kind:     global_buffer
      - .actual_access:  read_only
        .address_space:  global
        .offset:         48
        .size:           8
        .value_kind:     global_buffer
      - .actual_access:  write_only
        .address_space:  global
        .offset:         56
        .size:           8
        .value_kind:     global_buffer
      - .actual_access:  write_only
        .address_space:  global
        .offset:         64
        .size:           8
        .value_kind:     global_buffer
      - .actual_access:  write_only
        .address_space:  global
        .offset:         72
        .size:           8
        .value_kind:     global_buffer
      - .actual_access:  write_only
        .address_space:  global
        .offset:         80
        .size:           8
        .value_kind:     global_buffer
      - .actual_access:  read_only
        .address_space:  global
        .offset:         88
        .size:           8
        .value_kind:     global_buffer
      - .actual_access:  write_only
        .address_space:  global
        .offset:         96
        .size:           8
        .value_kind:     global_buffer
      - .actual_access:  read_only
        .address_space:  global
        .offset:         104
        .size:           8
        .value_kind:     global_buffer
      - .actual_access:  read_only
        .address_space:  global
        .offset:         112
        .size:           8
        .value_kind:     global_buffer
      - .actual_access:  write_only
        .address_space:  global
        .offset:         120
        .size:           8
        .value_kind:     global_buffer
      - .actual_access:  read_only
        .address_space:  global
        .offset:         128
        .size:           8
        .value_kind:     global_buffer
      - .address_space:  global
        .offset:         136
        .size:           8
        .value_kind:     global_buffer
      - .address_space:  global
        .offset:         144
        .size:           8
        .value_kind:     global_buffer
      - .address_space:  global
        .offset:         152
        .size:           8
        .value_kind:     global_buffer
      - .address_space:  global
        .offset:         160
        .size:           8
        .value_kind:     global_buffer
      - .address_space:  global
        .offset:         168
        .size:           8
        .value_kind:     global_buffer
      - .offset:         176
        .size:           4
        .value_kind:     hidden_block_count_x
      - .offset:         180
        .size:           4
        .value_kind:     hidden_block_count_y
      - .offset:         184
        .size:           4
        .value_kind:     hidden_block_count_z
      - .offset:         188
        .size:           2
        .value_kind:     hidden_group_size_x
      - .offset:         190
        .size:           2
        .value_kind:     hidden_group_size_y
      - .offset:         192
        .size:           2
        .value_kind:     hidden_group_size_z
      - .offset:         194
        .size:           2
        .value_kind:     hidden_remainder_x
      - .offset:         196
        .size:           2
        .value_kind:     hidden_remainder_y
      - .offset:         198
        .size:           2
        .value_kind:     hidden_remainder_z
      - .offset:         216
        .size:           8
        .value_kind:     hidden_global_offset_x
      - .offset:         224
        .size:           8
        .value_kind:     hidden_global_offset_y
      - .offset:         232
        .size:           8
        .value_kind:     hidden_global_offset_z
      - .offset:         240
        .size:           2
        .value_kind:     hidden_grid_dims
    .group_segment_fixed_size: 1024
    .kernarg_segment_align: 8
    .kernarg_segment_size: 432
    .language:       OpenCL C
    .language_version:
      - 2
      - 0
    .max_flat_workgroup_size: 1024
    .name:           _Z12prep_weightsPKfS0_S0_S0_S0_S0_S0_PDF16_S1_S1_S1_S0_S1_S0_S0_PfPKiPiS5_S5_S5_S5_
    .private_segment_fixed_size: 0
    .sgpr_count:     48
    .sgpr_spill_count: 0
    .symbol:         _Z12prep_weightsPKfS0_S0_S0_S0_S0_S0_PDF16_S1_S1_S1_S0_S1_S0_S0_PfPKiPiS5_S5_S5_S5_.kd
    .uniform_work_group_size: 1
    .uses_dynamic_stack: false
    .vgpr_count:     29
    .vgpr_spill_count: 0
    .wavefront_size: 64
  - .agpr_count:     0
    .args:
      - .actual_access:  read_only
        .address_space:  global
        .offset:         0
        .size:           8
        .value_kind:     global_buffer
      - .actual_access:  read_only
        .address_space:  global
        .offset:         8
        .size:           8
        .value_kind:     global_buffer
      - .actual_access:  read_only
        .address_space:  global
        .offset:         16
        .size:           8
        .value_kind:     global_buffer
      - .actual_access:  read_only
        .address_space:  global
        .offset:         24
        .size:           8
        .value_kind:     global_buffer
      - .actual_access:  read_only
        .address_space:  global
        .offset:         32
        .size:           8
        .value_kind:     global_buffer
      - .actual_access:  read_only
        .address_space:  global
        .offset:         40
        .size:           8
        .value_kind:     global_buffer
      - .actual_access:  read_only
        .address_space:  global
        .offset:         48
        .size:           8
        .value_kind:     global_buffer
      - .actual_access:  read_only
        .address_space:  global
        .offset:         56
        .size:           8
        .value_kind:     global_buffer
      - .actual_access:  write_only
        .address_space:  global
        .offset:         64
        .size:           8
        .value_kind:     global_buffer
      - .actual_access:  read_only
        .address_space:  global
        .offset:         72
        .size:           8
        .value_kind:     global_buffer
      - .actual_access:  read_only
        .address_space:  global
        .offset:         80
        .size:           8
        .value_kind:     global_buffer
      - .actual_access:  read_only
        .address_space:  global
        .offset:         88
        .size:           8
        .value_kind:     global_buffer
      - .actual_access:  read_only
        .address_space:  global
        .offset:         96
        .size:           8
        .value_kind:     global_buffer
      - .actual_access:  read_only
        .address_space:  global
        .offset:         104
        .size:           8
        .value_kind:     global_buffer
    .group_segment_fixed_size: 160512
    .kernarg_segment_align: 8
    .kernarg_segment_size: 112
    .language:       OpenCL C
    .language_version:
      - 2
      - 0
    .max_flat_workgroup_size: 512
    .name:           _Z8gru_mfmaPKiPKDF16_PKDv8_DF16_S5_S5_S5_S0_S0_PfPKfS8_S8_S8_S0_
    .private_segment_fixed_size: 0
    .sgpr_count:     27
    .sgpr_spill_count: 0
    .symbol:         _Z8gru_mfmaPKiPKDF16_PKDv8_DF16_S5_S5_S5_S0_S0_PfPKfS8_S8_S8_S0_.kd
    .uniform_work_group_size: 1
    .uses_dynamic_stack: false
    .vgpr_count:     256
    .vgpr_spill_count: 0
    .wavefront_size: 64
  - .agpr_count:     0
    .args:
      - .actual_access:  read_only
        .address_space:  global
        .offset:         0
        .size:           8
        .value_kind:     global_buffer
      - .actual_access:  read_only
        .address_space:  global
        .offset:         8
        .size:           8
        .value_kind:     global_buffer
      - .actual_access:  read_only
        .address_space:  global
        .offset:         16
        .size:           8
        .value_kind:     global_buffer
      - .actual_access:  read_only
        .address_space:  global
        .offset:         24
        .size:           8
        .value_kind:     global_buffer
      - .actual_access:  read_only
        .address_space:  global
        .offset:         32
        .size:           8
        .value_kind:     global_buffer
      - .actual_access:  read_only
        .address_space:  global
        .offset:         40
        .size:           8
        .value_kind:     global_buffer
      - .actual_access:  read_only
        .address_space:  global
        .offset:         48
        .size:           8
        .value_kind:     global_buffer
      - .actual_access:  read_only
        .address_space:  global
        .offset:         56
        .size:           8
        .value_kind:     global_buffer
      - .actual_access:  write_only
        .address_space:  global
        .offset:         64
        .size:           8
        .value_kind:     global_buffer
    .group_segment_fixed_size: 26624
    .kernarg_segment_align: 8
    .kernarg_segment_size: 72
    .language:       OpenCL C
    .language_version:
      - 2
      - 0
    .max_flat_workgroup_size: 256
    .name:           _Z10gcn_kernelPKiS0_S0_S0_PKfS2_S2_S2_Pf
    .private_segment_fixed_size: 0
    .sgpr_count:     42
    .sgpr_spill_count: 0
    .symbol:         _Z10gcn_kernelPKiS0_S0_S0_PKfS2_S2_S2_Pf.kd
    .uniform_work_group_size: 1
    .uses_dynamic_stack: false
    .vgpr_count:     96
    .vgpr_spill_count: 0
    .wavefront_size: 64
